# FFN weight-conversion loops: next item's loads now really stay in flight during the current item's transpose/convert/store (removed vmcnt(0) right after issuing them; vmcnt(8) only in a wave's first i
# speedup vs baseline: 1.0061x; 1.0061x over previous
.LBB0_280:
	v_lshrrev_b32_e32 v66, 3, v71
	v_mul_u32_u24_e32 v0, s16, v66
	v_lshlrev_b32_e32 v0, 2, v0
	v_lshl_add_u64 v[2:3], s[12:13], 0, v[0:1]
	v_lshlrev_b32_e32 v0, 2, v71
	v_or_b32_e32 v68, 8, v66
	v_and_b32_e32 v4, 28, v0
	v_mul_u32_u24_e32 v5, s16, v68
	v_lshlrev_b32_e32 v0, 2, v4
	v_lshlrev_b32_e32 v6, 2, v5
	v_mov_b32_e32 v7, v1
	v_lshl_add_u64 v[2:3], v[2:3], 0, v[0:1]
	v_lshl_add_u64 v[6:7], s[12:13], 0, v[6:7]
	v_or_b32_e32 v70, 16, v66
	v_lshl_add_u64 v[6:7], v[6:7], 0, v[0:1]
	global_load_dwordx4 v[62:65], v[2:3], off nt
	global_load_dwordx4 v[54:57], v[6:7], off nt
	v_mul_u32_u24_e32 v2, s16, v70
	v_or_b32_e32 v72, 24, v66
	v_lshlrev_b32_e32 v2, 2, v2
	v_mov_b32_e32 v3, v1
	v_mul_u32_u24_e32 v5, s16, v72
	v_lshl_add_u64 v[2:3], s[12:13], 0, v[2:3]
	v_lshlrev_b32_e32 v6, 2, v5
	v_mov_b32_e32 v7, v1
	v_lshl_add_u64 v[2:3], v[2:3], 0, v[0:1]
	v_lshl_add_u64 v[6:7], s[12:13], 0, v[6:7]
	v_or_b32_e32 v67, 32, v66
	v_lshl_add_u64 v[6:7], v[6:7], 0, v[0:1]
	global_load_dwordx4 v[58:61], v[2:3], off nt
	global_load_dwordx4 v[46:49], v[6:7], off nt
	v_mul_u32_u24_e32 v2, s16, v67
	v_or_b32_e32 v73, 40, v66
	v_lshlrev_b32_e32 v2, 2, v2
	v_mov_b32_e32 v3, v1
	v_mul_u32_u24_e32 v5, s16, v73
	v_lshl_add_u64 v[2:3], s[12:13], 0, v[2:3]
	v_lshlrev_b32_e32 v6, 2, v5
	v_mov_b32_e32 v7, v1
	v_lshl_add_u64 v[2:3], v[2:3], 0, v[0:1]
	v_lshl_add_u64 v[6:7], s[12:13], 0, v[6:7]
	v_or_b32_e32 v80, 48, v66
	v_lshl_add_u64 v[6:7], v[6:7], 0, v[0:1]
	global_load_dwordx4 v[50:53], v[2:3], off nt
	global_load_dwordx4 v[38:41], v[6:7], off nt
	v_mul_u32_u24_e32 v2, s16, v80
	v_or_b32_e32 v81, 56, v66
	v_lshlrev_b32_e32 v2, 2, v2
	v_mov_b32_e32 v3, v1
	v_mul_u32_u24_e32 v5, s16, v81
	v_lshl_add_u64 v[2:3], s[12:13], 0, v[2:3]
	v_lshlrev_b32_e32 v6, 2, v5
	v_mov_b32_e32 v7, v1
	v_lshl_add_u64 v[2:3], v[2:3], 0, v[0:1]
	v_lshl_add_u64 v[6:7], s[12:13], 0, v[6:7]
	v_lshl_add_u64 v[6:7], v[6:7], 0, v[0:1]
	global_load_dwordx4 v[42:45], v[2:3], off nt
	global_load_dwordx4 v[34:37], v[6:7], off nt
	v_and_b32_e32 v0, 7, v69
	v_lshlrev_b32_e32 v74, 4, v0
	v_readlane_b32 s4, v252, 4
	v_lshlrev_b32_e32 v76, 3, v0
	v_mul_u32_u24_e32 v0, 0x420, v0
	v_lshlrev_b32_e32 v5, 2, v66
	v_add_u32_e32 v2, s4, v74
	v_mul_u32_u24_e32 v3, 0x84, v66
	v_add3_u32 v82, s4, v0, v5
	v_readlane_b32 s4, v254, 36
	v_mov_b32_e32 v77, v1
	v_mov_b32_e32 v75, v1
	v_lshlrev_b32_e32 v78, 2, v4
	v_add_u32_e32 v83, v2, v3
	v_readlane_b32 s36, v254, 30
	v_readlane_b32 s37, v254, 29
	s_mov_b32 s40, s4
	s_mov_b32 s100, s4
	v_readlane_b32 s5, v254, 37
	s_branch .LBB0_282

.LBB0_288:
	v_mul_u32_u24_e32 v0, s20, v66
	v_lshlrev_b32_e32 v0, 2, v0
	v_lshl_add_u64 v[2:3], s[18:19], 0, v[0:1]
	v_mul_u32_u24_e32 v0, s20, v68
	v_lshlrev_b32_e32 v0, 2, v0
	v_lshl_add_u64 v[4:5], s[18:19], 0, v[0:1]
	v_mul_u32_u24_e32 v0, s20, v70
	v_lshlrev_b32_e32 v0, 2, v0
	v_lshl_add_u64 v[10:11], s[18:19], 0, v[0:1]
	v_mul_u32_u24_e32 v0, s20, v72
	v_lshlrev_b32_e32 v0, 2, v0
	v_lshl_add_u64 v[12:13], s[18:19], 0, v[0:1]
	v_mul_u32_u24_e32 v0, s20, v67
	v_lshlrev_b32_e32 v0, 2, v0
	v_lshl_add_u64 v[18:19], s[18:19], 0, v[0:1]
	v_mul_u32_u24_e32 v0, s20, v73
	v_lshlrev_b32_e32 v0, 2, v0
	v_lshl_add_u64 v[20:21], s[18:19], 0, v[0:1]
	v_mul_u32_u24_e32 v0, s20, v80
	v_lshlrev_b32_e32 v0, 2, v0
	v_lshl_add_u64 v[26:27], s[18:19], 0, v[0:1]
	v_mul_u32_u24_e32 v0, s20, v81
	v_lshlrev_b32_e32 v0, 2, v0
	v_mov_b32_e32 v79, v1
	v_lshl_add_u64 v[28:29], s[18:19], 0, v[0:1]
	v_lshl_add_u64 v[2:3], v[2:3], 0, v[78:79]
	v_lshl_add_u64 v[4:5], v[4:5], 0, v[78:79]
	v_lshl_add_u64 v[10:11], v[10:11], 0, v[78:79]
	v_lshl_add_u64 v[12:13], v[12:13], 0, v[78:79]
	v_lshl_add_u64 v[18:19], v[18:19], 0, v[78:79]
	v_lshl_add_u64 v[20:21], v[20:21], 0, v[78:79]
	v_lshl_add_u64 v[26:27], v[26:27], 0, v[78:79]
	v_lshl_add_u64 v[28:29], v[28:29], 0, v[78:79]
	global_load_dwordx4 v[6:9], v[2:3], off nt
	s_nop 0
	global_load_dwordx4 v[2:5], v[4:5], off nt
	s_nop 0
	global_load_dwordx4 v[14:17], v[10:11], off nt
	s_nop 0
	global_load_dwordx4 v[10:13], v[12:13], off nt
	s_nop 0
	global_load_dwordx4 v[22:25], v[18:19], off nt
	s_nop 0
	global_load_dwordx4 v[18:21], v[20:21], off nt
	s_nop 0
	global_load_dwordx4 v[30:33], v[26:27], off nt
	s_nop 0
	global_load_dwordx4 v[26:29], v[28:29], off nt
	s_cmp_lg_u32 s40, s100
	s_cbranch_scc1 .LBB0_289
	s_waitcnt vmcnt(8)
	s_branch .LBB0_289

.LBB0_289:
	v_add_u32_e32 v0, 0x420, v83

	ds_write2_b32 v83, v62, v63 offset1:1
	ds_write2_b32 v83, v64, v65 offset0:2 offset1:3
	ds_write2_b32 v0, v54, v55 offset1:1
	v_add_u32_e32 v0, 0x428, v83
	ds_write2_b32 v0, v56, v57 offset1:1
	v_add_u32_e32 v0, 0x840, v83
	ds_write2_b32 v0, v58, v59 offset1:1
	v_add_u32_e32 v0, 0x848, v83
	ds_write2_b32 v0, v60, v61 offset1:1
	v_add_u32_e32 v0, 0xc60, v83
	ds_write2_b32 v0, v46, v47 offset1:1
	v_add_u32_e32 v0, 0xc68, v83
	ds_write2_b32 v0, v48, v49 offset1:1
	v_add_u32_e32 v0, 0x1080, v83
	ds_write2_b32 v0, v50, v51 offset1:1
	v_add_u32_e32 v0, 0x1088, v83
	ds_write2_b32 v0, v52, v53 offset1:1
	v_add_u32_e32 v0, 0x14a0, v83
	ds_write2_b32 v0, v38, v39 offset1:1
	v_add_u32_e32 v0, 0x14a8, v83
	ds_write2_b32 v0, v40, v41 offset1:1
	v_add_u32_e32 v0, 0x18c0, v83
	ds_write2_b32 v0, v42, v43 offset1:1
	v_add_u32_e32 v0, 0x18c8, v83
	ds_write2_b32 v0, v44, v45 offset1:1
	v_add_u32_e32 v0, 0x1ce0, v83
	ds_write2_b32 v0, v34, v35 offset1:1
	v_add_u32_e32 v0, 0x1ce8, v83
	ds_write2_b32 v0, v36, v37 offset1:1
	s_waitcnt lgkmcnt(0)
	ds_read2_b32 v[34:35], v82 offset1:33
	ds_read2_b32 v[36:37], v82 offset0:66 offset1:99
	ds_read2_b32 v[42:43], v82 offset0:132 offset1:165
	ds_read2_b32 v[44:45], v82 offset0:198 offset1:231
	s_mov_b64 s[22:23], -1
	s_waitcnt lgkmcnt(3)
	v_pk_mul_f32 v[40:41], s[14:15], v[34:35] op_sel_hi:[0,1]
	s_waitcnt lgkmcnt(2)
	v_pk_mul_f32 v[38:39], s[14:15], v[36:37] op_sel_hi:[0,1]
	s_waitcnt lgkmcnt(1)
	v_pk_mul_f32 v[36:37], s[14:15], v[42:43] op_sel_hi:[0,1]
	s_waitcnt lgkmcnt(0)
	v_pk_mul_f32 v[34:35], s[14:15], v[44:45] op_sel_hi:[0,1]
	s_mov_b64 s[18:19], 0
	s_cmp_lt_i32 s44, 2
	s_mov_b64 s[20:21], 0
	s_cbranch_scc1 .LBB0_295
	s_cmp_eq_u32 s44, 2
	s_mov_b64 s[20:21], -1
	s_cbranch_scc0 .LBB0_292
	v_rndne_f32_e32 v42, v41
	v_rndne_f32_e32 v43, v38
	v_rndne_f32_e32 v0, v40
	v_cvt_i32_f32_e32 v42, v42
	v_cvt_i32_f32_e32 v43, v43
	v_rndne_f32_e32 v44, v39
	v_cvt_i32_f32_e32 v0, v0
	v_cvt_i32_f32_e32 v44, v44
	v_med3_i32 v42, v42, s84, v236
	v_med3_i32 v43, v43, s84, v236
	v_med3_i32 v0, v0, s84, v236
	v_med3_i32 v44, v44, s84, v236
	v_lshlrev_b32_e32 v42, 8, v42
	v_lshlrev_b32_e32 v43, 16, v43
	v_and_b32_e32 v42, 0xff00, v42
	v_and_b32_e32 v43, 0xff0000, v43
	v_perm_b32 v0, v44, v0, s60
	v_or3_b32 v42, v0, v42, v43
	v_rndne_f32_e32 v43, v37
	v_rndne_f32_e32 v44, v34
	v_rndne_f32_e32 v0, v36
	v_cvt_i32_f32_e32 v43, v43
	v_cvt_i32_f32_e32 v44, v44
	v_rndne_f32_e32 v45, v35
	v_cvt_i32_f32_e32 v0, v0
	v_cvt_i32_f32_e32 v45, v45
	v_med3_i32 v43, v43, s84, v236
	v_med3_i32 v44, v44, s84, v236
	v_med3_i32 v0, v0, s84, v236
	v_med3_i32 v45, v45, s84, v236
	v_lshlrev_b32_e32 v43, 8, v43
	v_lshlrev_b32_e32 v44, 16, v44
	v_and_b32_e32 v43, 0xff00, v43
	v_and_b32_e32 v44, 0xff0000, v44
	v_perm_b32 v0, v45, v0, s60
	v_or3_b32 v43, v0, v43, v44
	v_mov_b64_e32 v[44:45], s[10:11]
	v_mad_i64_i32 v[44:45], s[4:5], s41, v66, v[44:45]
	v_lshl_add_u64 v[44:45], v[44:45], 0, v[76:77]
	global_store_dwordx2 v[44:45], v[42:43], off
	s_mov_b64 s[20:21], 0

.LBB0_329:
	s_waitcnt lgkmcnt(0)
	s_andn2_b64 vcc, exec, s[16:17]
	s_mov_b64 s[10:11], -1
	s_cbranch_vccnz .LBB0_281
	v_readlane_b32 s4, v254, 31
	s_add_i32 s40, s40, s42
	s_add_i32 s37, s37, s65
	s_add_i32 s36, s36, s4
	s_mov_b64 s[10:11], 0
	s_waitcnt vmcnt(4)
	v_mov_b32_e32 v37, v29
	v_mov_b32_e32 v36, v28
	v_mov_b32_e32 v35, v27
	v_mov_b32_e32 v34, v26
	v_mov_b32_e32 v45, v33
	v_mov_b32_e32 v44, v32
	v_mov_b32_e32 v43, v31
	v_mov_b32_e32 v42, v30
	v_mov_b32_e32 v41, v21
	v_mov_b32_e32 v40, v20
	v_mov_b32_e32 v39, v19
	v_mov_b32_e32 v38, v18
	v_mov_b32_e32 v53, v25
	v_mov_b32_e32 v52, v24
	v_mov_b32_e32 v51, v23
	v_mov_b32_e32 v50, v22
	v_mov_b32_e32 v49, v13
	v_mov_b32_e32 v48, v12
	v_mov_b32_e32 v47, v11
	v_mov_b32_e32 v46, v10
	v_mov_b32_e32 v61, v17
	v_mov_b32_e32 v60, v16
	v_mov_b32_e32 v59, v15
	v_mov_b32_e32 v58, v14
	v_mov_b32_e32 v57, v5
	v_mov_b32_e32 v56, v4
	v_mov_b32_e32 v55, v3
	v_mov_b32_e32 v54, v2
	v_mov_b32_e32 v65, v9
	v_mov_b32_e32 v64, v8
	v_mov_b32_e32 v63, v7
	v_mov_b32_e32 v62, v6
	s_branch .LBB0_281

.LBB0_339:
	v_lshrrev_b32_e32 v68, 3, v71
	v_mul_u32_u24_e32 v0, s12, v68
	v_lshlrev_b32_e32 v0, 2, v0
	v_lshl_add_u64 v[2:3], s[10:11], 0, v[0:1]
	v_lshlrev_b32_e32 v0, 2, v71
	v_or_b32_e32 v70, 8, v68
	v_and_b32_e32 v4, 28, v0
	v_mul_u32_u24_e32 v5, s12, v70
	v_lshlrev_b32_e32 v0, 2, v4
	v_lshlrev_b32_e32 v6, 2, v5
	v_mov_b32_e32 v7, v1
	v_lshl_add_u64 v[2:3], v[2:3], 0, v[0:1]
	v_lshl_add_u64 v[6:7], s[10:11], 0, v[6:7]
	v_or_b32_e32 v72, 16, v68
	v_lshl_add_u64 v[6:7], v[6:7], 0, v[0:1]
	global_load_dwordx4 v[62:65], v[2:3], off nt
	global_load_dwordx4 v[54:57], v[6:7], off nt
	v_mul_u32_u24_e32 v2, s12, v72
	v_or_b32_e32 v74, 24, v68
	v_lshlrev_b32_e32 v2, 2, v2
	v_mov_b32_e32 v3, v1
	v_mul_u32_u24_e32 v5, s12, v74
	v_lshl_add_u64 v[2:3], s[10:11], 0, v[2:3]
	v_lshlrev_b32_e32 v6, 2, v5
	v_mov_b32_e32 v7, v1
	v_lshl_add_u64 v[2:3], v[2:3], 0, v[0:1]
	v_lshl_add_u64 v[6:7], s[10:11], 0, v[6:7]
	v_or_b32_e32 v71, 32, v68
	v_lshl_add_u64 v[6:7], v[6:7], 0, v[0:1]
	global_load_dwordx4 v[58:61], v[2:3], off nt
	global_load_dwordx4 v[46:49], v[6:7], off nt
	v_mul_u32_u24_e32 v2, s12, v71
	v_or_b32_e32 v75, 40, v68
	v_lshlrev_b32_e32 v2, 2, v2
	v_mov_b32_e32 v3, v1
	v_mul_u32_u24_e32 v5, s12, v75
	v_lshl_add_u64 v[2:3], s[10:11], 0, v[2:3]
	v_lshlrev_b32_e32 v6, 2, v5
	v_mov_b32_e32 v7, v1
	v_lshl_add_u64 v[2:3], v[2:3], 0, v[0:1]
	v_lshl_add_u64 v[6:7], s[10:11], 0, v[6:7]
	v_or_b32_e32 v88, 48, v68
	v_lshl_add_u64 v[6:7], v[6:7], 0, v[0:1]
	global_load_dwordx4 v[50:53], v[2:3], off nt
	global_load_dwordx4 v[38:41], v[6:7], off nt
	v_mul_u32_u24_e32 v2, s12, v88
	v_or_b32_e32 v89, 56, v68
	v_lshlrev_b32_e32 v2, 2, v2
	v_mov_b32_e32 v3, v1
	v_mul_u32_u24_e32 v5, s12, v89
	v_lshl_add_u64 v[2:3], s[10:11], 0, v[2:3]
	v_lshlrev_b32_e32 v6, 2, v5
	v_mov_b32_e32 v7, v1
	v_lshl_add_u64 v[2:3], v[2:3], 0, v[0:1]
	v_lshl_add_u64 v[6:7], s[10:11], 0, v[6:7]
	v_lshl_add_u64 v[6:7], v[6:7], 0, v[0:1]
	global_load_dwordx4 v[42:45], v[2:3], off nt
	global_load_dwordx4 v[34:37], v[6:7], off nt
	v_and_b32_e32 v0, 7, v69
	v_lshlrev_b32_e32 v76, 4, v0
	v_readlane_b32 s4, v252, 4
	v_lshlrev_b32_e32 v78, 3, v0
	v_mul_u32_u24_e32 v0, 0x420, v0
	v_lshlrev_b32_e32 v2, 2, v68
	v_add_u32_e32 v5, s4, v76
	v_mul_u32_u24_e32 v6, 0x84, v68
	v_add3_u32 v69, s4, v0, v2
	v_readlane_b32 s4, v254, 36
	v_mov_b32_e32 v79, v1
	v_mov_b32_e32 v77, v1
	v_lshlrev_b32_e32 v82, 2, v4
	v_add_u32_e32 v90, v5, v6
	v_readlane_b32 s25, v254, 30
	v_readlane_b32 s26, v254, 29
	s_mov_b32 s27, s4
	s_mov_b32 s100, s4
	v_readlane_b32 s5, v254, 37
	s_branch .LBB0_341

.LBB0_347:
	v_mul_u32_u24_e32 v0, s12, v68
	v_lshlrev_b32_e32 v0, 2, v0
	v_lshl_add_u64 v[2:3], s[10:11], 0, v[0:1]
	v_mul_u32_u24_e32 v0, s12, v70
	v_lshlrev_b32_e32 v0, 2, v0
	v_lshl_add_u64 v[4:5], s[10:11], 0, v[0:1]
	v_mul_u32_u24_e32 v0, s12, v72
	v_lshlrev_b32_e32 v0, 2, v0
	v_lshl_add_u64 v[10:11], s[10:11], 0, v[0:1]
	v_mul_u32_u24_e32 v0, s12, v74
	v_lshlrev_b32_e32 v0, 2, v0
	v_lshl_add_u64 v[12:13], s[10:11], 0, v[0:1]
	v_mul_u32_u24_e32 v0, s12, v71
	v_lshlrev_b32_e32 v0, 2, v0
	v_lshl_add_u64 v[18:19], s[10:11], 0, v[0:1]
	v_mul_u32_u24_e32 v0, s12, v75
	v_lshlrev_b32_e32 v0, 2, v0
	v_lshl_add_u64 v[20:21], s[10:11], 0, v[0:1]
	v_mul_u32_u24_e32 v0, s12, v88
	v_lshlrev_b32_e32 v0, 2, v0
	v_lshl_add_u64 v[26:27], s[10:11], 0, v[0:1]
	v_mul_u32_u24_e32 v0, s12, v89
	v_lshlrev_b32_e32 v0, 2, v0
	v_mov_b32_e32 v83, v1
	v_lshl_add_u64 v[28:29], s[10:11], 0, v[0:1]
	v_lshl_add_u64 v[2:3], v[2:3], 0, v[82:83]
	v_lshl_add_u64 v[4:5], v[4:5], 0, v[82:83]
	v_lshl_add_u64 v[10:11], v[10:11], 0, v[82:83]
	v_lshl_add_u64 v[12:13], v[12:13], 0, v[82:83]
	v_lshl_add_u64 v[18:19], v[18:19], 0, v[82:83]
	v_lshl_add_u64 v[20:21], v[20:21], 0, v[82:83]
	v_lshl_add_u64 v[26:27], v[26:27], 0, v[82:83]
	v_lshl_add_u64 v[28:29], v[28:29], 0, v[82:83]
	global_load_dwordx4 v[6:9], v[2:3], off nt
	s_nop 0
	global_load_dwordx4 v[2:5], v[4:5], off nt
	s_nop 0
	global_load_dwordx4 v[14:17], v[10:11], off nt
	s_nop 0
	global_load_dwordx4 v[10:13], v[12:13], off nt
	s_nop 0
	global_load_dwordx4 v[22:25], v[18:19], off nt
	s_nop 0
	global_load_dwordx4 v[18:21], v[20:21], off nt
	s_nop 0
	global_load_dwordx4 v[30:33], v[26:27], off nt
	s_nop 0
	global_load_dwordx4 v[26:29], v[28:29], off nt
	s_cmp_lg_u32 s27, s100
	s_cbranch_scc1 .LBB0_348
	s_waitcnt vmcnt(8)
	s_branch .LBB0_348

.LBB0_348:
	v_add_u32_e32 v0, 0x420, v90

	ds_write2_b32 v90, v62, v63 offset1:1
	ds_write2_b32 v90, v64, v65 offset0:2 offset1:3
	ds_write2_b32 v0, v54, v55 offset1:1
	v_add_u32_e32 v0, 0x428, v90
	ds_write2_b32 v0, v56, v57 offset1:1
	v_add_u32_e32 v0, 0x840, v90
	ds_write2_b32 v0, v58, v59 offset1:1
	v_add_u32_e32 v0, 0x848, v90
	ds_write2_b32 v0, v60, v61 offset1:1
	v_add_u32_e32 v0, 0xc60, v90
	ds_write2_b32 v0, v46, v47 offset1:1
	v_add_u32_e32 v0, 0xc68, v90
	ds_write2_b32 v0, v48, v49 offset1:1
	v_add_u32_e32 v0, 0x1080, v90
	ds_write2_b32 v0, v50, v51 offset1:1
	v_add_u32_e32 v0, 0x1088, v90
	ds_write2_b32 v0, v52, v53 offset1:1
	v_add_u32_e32 v0, 0x14a0, v90
	ds_write2_b32 v0, v38, v39 offset1:1
	v_add_u32_e32 v0, 0x14a8, v90
	ds_write2_b32 v0, v40, v41 offset1:1
	v_add_u32_e32 v0, 0x18c0, v90
	ds_write2_b32 v0, v42, v43 offset1:1
	v_add_u32_e32 v0, 0x18c8, v90
	ds_write2_b32 v0, v44, v45 offset1:1
	v_add_u32_e32 v0, 0x1ce0, v90
	ds_write2_b32 v0, v34, v35 offset1:1
	v_add_u32_e32 v0, 0x1ce8, v90
	ds_write2_b32 v0, v36, v37 offset1:1
	s_waitcnt lgkmcnt(0)
	ds_read2_b32 v[34:35], v69 offset1:33
	ds_read2_b32 v[36:37], v69 offset0:66 offset1:99
	ds_read2_b32 v[42:43], v69 offset0:132 offset1:165
	ds_read2_b32 v[44:45], v69 offset0:198 offset1:231
	s_mov_b64 s[14:15], -1
	s_waitcnt lgkmcnt(3)
	v_pk_mul_f32 v[40:41], v[86:87], v[34:35] op_sel_hi:[0,1]
	s_waitcnt lgkmcnt(2)
	v_pk_mul_f32 v[38:39], v[86:87], v[36:37] op_sel_hi:[0,1]
	s_waitcnt lgkmcnt(1)
	v_pk_mul_f32 v[36:37], v[86:87], v[42:43] op_sel_hi:[0,1]
	s_waitcnt lgkmcnt(0)
	v_pk_mul_f32 v[34:35], v[86:87], v[44:45] op_sel_hi:[0,1]
	s_mov_b64 s[10:11], 0
	s_cmp_lt_i32 s28, 2
	s_mov_b64 s[12:13], 0
	s_cbranch_scc1 .LBB0_354
	s_cmp_eq_u32 s28, 2
	s_mov_b64 s[12:13], -1
	s_cbranch_scc0 .LBB0_351
	v_rndne_f32_e32 v42, v41
	v_rndne_f32_e32 v43, v38
	v_rndne_f32_e32 v0, v40
	v_cvt_i32_f32_e32 v42, v42
	v_cvt_i32_f32_e32 v43, v43
	v_rndne_f32_e32 v44, v39
	v_cvt_i32_f32_e32 v0, v0
	v_cvt_i32_f32_e32 v44, v44
	v_med3_i32 v42, v42, s84, v236
	v_med3_i32 v43, v43, s84, v236
	v_med3_i32 v0, v0, s84, v236
	v_med3_i32 v44, v44, s84, v236
	v_lshlrev_b32_e32 v42, 8, v42
	v_lshlrev_b32_e32 v43, 16, v43
	v_and_b32_e32 v42, 0xff00, v42
	v_and_b32_e32 v43, 0xff0000, v43
	v_perm_b32 v0, v44, v0, s60
	v_or3_b32 v42, v0, v42, v43
	v_rndne_f32_e32 v43, v37
	v_rndne_f32_e32 v44, v34
	v_rndne_f32_e32 v0, v36
	v_cvt_i32_f32_e32 v43, v43
	v_cvt_i32_f32_e32 v44, v44
	v_rndne_f32_e32 v45, v35
	v_cvt_i32_f32_e32 v0, v0
	v_cvt_i32_f32_e32 v45, v45
	v_med3_i32 v43, v43, s84, v236
	v_med3_i32 v44, v44, s84, v236
	v_med3_i32 v0, v0, s84, v236
	v_med3_i32 v45, v45, s84, v236
	v_lshlrev_b32_e32 v43, 8, v43
	v_lshlrev_b32_e32 v44, 16, v44
	v_and_b32_e32 v43, 0xff00, v43
	v_and_b32_e32 v44, 0xff0000, v44
	v_perm_b32 v0, v45, v0, s60
	v_or3_b32 v43, v0, v43, v44
	v_mad_i64_i32 v[44:45], s[4:5], v91, v68, v[80:81]
	v_lshl_add_u64 v[44:45], v[44:45], 0, v[78:79]
	global_store_dwordx2 v[44:45], v[42:43], off
	s_mov_b64 s[12:13], 0

.LBB0_388:
	s_waitcnt lgkmcnt(0)
	s_andn2_b64 vcc, exec, s[6:7]
	s_mov_b64 s[6:7], -1
	s_cbranch_vccnz .LBB0_340
	v_readlane_b32 s4, v254, 31
	s_add_i32 s27, s27, s42
	s_add_i32 s26, s26, s65
	s_add_i32 s25, s25, s4
	s_mov_b64 s[6:7], 0
	s_waitcnt vmcnt(4)
	v_mov_b32_e32 v37, v29
	v_mov_b32_e32 v36, v28
	v_mov_b32_e32 v35, v27
	v_mov_b32_e32 v34, v26
	v_mov_b32_e32 v45, v33
	v_mov_b32_e32 v44, v32
	v_mov_b32_e32 v43, v31
	v_mov_b32_e32 v42, v30
	v_mov_b32_e32 v41, v21
	v_mov_b32_e32 v40, v20
	v_mov_b32_e32 v39, v19
	v_mov_b32_e32 v38, v18
	v_mov_b32_e32 v53, v25
	v_mov_b32_e32 v52, v24
	v_mov_b32_e32 v51, v23
	v_mov_b32_e32 v50, v22
	v_mov_b32_e32 v49, v13
	v_mov_b32_e32 v48, v12
	v_mov_b32_e32 v47, v11
	v_mov_b32_e32 v46, v10
	v_mov_b32_e32 v61, v17
	v_mov_b32_e32 v60, v16
	v_mov_b32_e32 v59, v15
	v_mov_b32_e32 v58, v14
	v_mov_b32_e32 v57, v5
	v_mov_b32_e32 v56, v4
	v_mov_b32_e32 v55, v3
	v_mov_b32_e32 v54, v2
	v_mov_b32_e32 v65, v9
	v_mov_b32_e32 v64, v8
	v_mov_b32_e32 v63, v7
	v_mov_b32_e32 v62, v6
	s_branch .LBB0_340

.LBB0_623:
	v_lshrrev_b32_e32 v66, 3, v71
	v_mul_u32_u24_e32 v0, s16, v66
	v_lshlrev_b32_e32 v0, 2, v0
	v_lshl_add_u64 v[2:3], s[12:13], 0, v[0:1]
	v_lshlrev_b32_e32 v0, 2, v71
	v_or_b32_e32 v68, 8, v66
	v_and_b32_e32 v4, 28, v0
	v_mul_u32_u24_e32 v5, s16, v68
	v_lshlrev_b32_e32 v0, 2, v4
	v_lshlrev_b32_e32 v6, 2, v5
	v_mov_b32_e32 v7, v1
	v_lshl_add_u64 v[2:3], v[2:3], 0, v[0:1]
	v_lshl_add_u64 v[6:7], s[12:13], 0, v[6:7]
	v_or_b32_e32 v70, 16, v66
	v_lshl_add_u64 v[6:7], v[6:7], 0, v[0:1]
	global_load_dwordx4 v[62:65], v[2:3], off nt
	global_load_dwordx4 v[54:57], v[6:7], off nt
	v_mul_u32_u24_e32 v2, s16, v70
	v_or_b32_e32 v72, 24, v66
	v_lshlrev_b32_e32 v2, 2, v2
	v_mov_b32_e32 v3, v1
	v_mul_u32_u24_e32 v5, s16, v72
	v_lshl_add_u64 v[2:3], s[12:13], 0, v[2:3]
	v_lshlrev_b32_e32 v6, 2, v5
	v_mov_b32_e32 v7, v1
	v_lshl_add_u64 v[2:3], v[2:3], 0, v[0:1]
	v_lshl_add_u64 v[6:7], s[12:13], 0, v[6:7]
	v_or_b32_e32 v67, 32, v66
	v_lshl_add_u64 v[6:7], v[6:7], 0, v[0:1]
	global_load_dwordx4 v[58:61], v[2:3], off nt
	global_load_dwordx4 v[46:49], v[6:7], off nt
	v_mul_u32_u24_e32 v2, s16, v67
	v_or_b32_e32 v73, 40, v66
	v_lshlrev_b32_e32 v2, 2, v2
	v_mov_b32_e32 v3, v1
	v_mul_u32_u24_e32 v5, s16, v73
	v_lshl_add_u64 v[2:3], s[12:13], 0, v[2:3]
	v_lshlrev_b32_e32 v6, 2, v5
	v_mov_b32_e32 v7, v1
	v_lshl_add_u64 v[2:3], v[2:3], 0, v[0:1]
	v_lshl_add_u64 v[6:7], s[12:13], 0, v[6:7]
	v_or_b32_e32 v80, 48, v66
	v_lshl_add_u64 v[6:7], v[6:7], 0, v[0:1]
	global_load_dwordx4 v[50:53], v[2:3], off nt
	global_load_dwordx4 v[38:41], v[6:7], off nt
	v_mul_u32_u24_e32 v2, s16, v80
	v_or_b32_e32 v81, 56, v66
	v_lshlrev_b32_e32 v2, 2, v2
	v_mov_b32_e32 v3, v1
	v_mul_u32_u24_e32 v5, s16, v81
	v_lshl_add_u64 v[2:3], s[12:13], 0, v[2:3]
	v_lshlrev_b32_e32 v6, 2, v5
	v_mov_b32_e32 v7, v1
	v_lshl_add_u64 v[2:3], v[2:3], 0, v[0:1]
	v_lshl_add_u64 v[6:7], s[12:13], 0, v[6:7]
	v_lshl_add_u64 v[6:7], v[6:7], 0, v[0:1]
	global_load_dwordx4 v[42:45], v[2:3], off nt
	global_load_dwordx4 v[34:37], v[6:7], off nt
	v_and_b32_e32 v0, 7, v69
	v_lshlrev_b32_e32 v74, 4, v0
	v_readlane_b32 s4, v252, 4
	v_lshlrev_b32_e32 v76, 3, v0
	v_mul_u32_u24_e32 v0, 0x420, v0
	v_lshlrev_b32_e32 v5, 2, v66
	v_add_u32_e32 v2, s4, v74
	v_mul_u32_u24_e32 v3, 0x84, v66
	v_add3_u32 v82, s4, v0, v5
	v_readlane_b32 s4, v254, 36
	v_mov_b32_e32 v77, v1
	v_mov_b32_e32 v75, v1
	v_lshlrev_b32_e32 v78, 2, v4
	v_add_u32_e32 v83, v2, v3
	v_readlane_b32 s35, v254, 30
	v_readlane_b32 s36, v254, 29
	s_mov_b32 s37, s4
	s_mov_b32 s100, s4
	v_readlane_b32 s5, v254, 37
	s_branch .LBB0_625

.LBB0_631:
	v_mul_u32_u24_e32 v0, s20, v66
	v_lshlrev_b32_e32 v0, 2, v0
	v_lshl_add_u64 v[2:3], s[18:19], 0, v[0:1]
	v_mul_u32_u24_e32 v0, s20, v68
	v_lshlrev_b32_e32 v0, 2, v0
	v_lshl_add_u64 v[4:5], s[18:19], 0, v[0:1]
	v_mul_u32_u24_e32 v0, s20, v70
	v_lshlrev_b32_e32 v0, 2, v0
	v_lshl_add_u64 v[10:11], s[18:19], 0, v[0:1]
	v_mul_u32_u24_e32 v0, s20, v72
	v_lshlrev_b32_e32 v0, 2, v0
	v_lshl_add_u64 v[12:13], s[18:19], 0, v[0:1]
	v_mul_u32_u24_e32 v0, s20, v67
	v_lshlrev_b32_e32 v0, 2, v0
	v_lshl_add_u64 v[18:19], s[18:19], 0, v[0:1]
	v_mul_u32_u24_e32 v0, s20, v73
	v_lshlrev_b32_e32 v0, 2, v0
	v_lshl_add_u64 v[20:21], s[18:19], 0, v[0:1]
	v_mul_u32_u24_e32 v0, s20, v80
	v_lshlrev_b32_e32 v0, 2, v0
	v_lshl_add_u64 v[26:27], s[18:19], 0, v[0:1]
	v_mul_u32_u24_e32 v0, s20, v81
	v_lshlrev_b32_e32 v0, 2, v0
	v_mov_b32_e32 v79, v1
	v_lshl_add_u64 v[28:29], s[18:19], 0, v[0:1]
	v_lshl_add_u64 v[2:3], v[2:3], 0, v[78:79]
	v_lshl_add_u64 v[4:5], v[4:5], 0, v[78:79]
	v_lshl_add_u64 v[10:11], v[10:11], 0, v[78:79]
	v_lshl_add_u64 v[12:13], v[12:13], 0, v[78:79]
	v_lshl_add_u64 v[18:19], v[18:19], 0, v[78:79]
	v_lshl_add_u64 v[20:21], v[20:21], 0, v[78:79]
	v_lshl_add_u64 v[26:27], v[26:27], 0, v[78:79]
	v_lshl_add_u64 v[28:29], v[28:29], 0, v[78:79]
	global_load_dwordx4 v[6:9], v[2:3], off nt
	s_nop 0
	global_load_dwordx4 v[2:5], v[4:5], off nt
	s_nop 0
	global_load_dwordx4 v[14:17], v[10:11], off nt
	s_nop 0
	global_load_dwordx4 v[10:13], v[12:13], off nt
	s_nop 0
	global_load_dwordx4 v[22:25], v[18:19], off nt
	s_nop 0
	global_load_dwordx4 v[18:21], v[20:21], off nt
	s_nop 0
	global_load_dwordx4 v[30:33], v[26:27], off nt
	s_nop 0
	global_load_dwordx4 v[26:29], v[28:29], off nt
	s_cmp_lg_u32 s37, s100
	s_cbranch_scc1 .LBB0_632
	s_waitcnt vmcnt(8)
	s_branch .LBB0_632

.LBB0_632:
	v_add_u32_e32 v0, 0x420, v83

	ds_write2_b32 v83, v62, v63 offset1:1
	ds_write2_b32 v83, v64, v65 offset0:2 offset1:3

	ds_write2_b32 v0, v54, v55 offset1:1
	v_add_u32_e32 v0, 0x428, v83
	ds_write2_b32 v0, v56, v57 offset1:1
	v_add_u32_e32 v0, 0x840, v83

	ds_write2_b32 v0, v58, v59 offset1:1
	v_add_u32_e32 v0, 0x848, v83
	ds_write2_b32 v0, v60, v61 offset1:1
	v_add_u32_e32 v0, 0xc60, v83

	ds_write2_b32 v0, v46, v47 offset1:1
	v_add_u32_e32 v0, 0xc68, v83
	ds_write2_b32 v0, v48, v49 offset1:1
	v_add_u32_e32 v0, 0x1080, v83

	ds_write2_b32 v0, v50, v51 offset1:1
	v_add_u32_e32 v0, 0x1088, v83
	ds_write2_b32 v0, v52, v53 offset1:1
	v_add_u32_e32 v0, 0x14a0, v83

	ds_write2_b32 v0, v38, v39 offset1:1
	v_add_u32_e32 v0, 0x14a8, v83
	ds_write2_b32 v0, v40, v41 offset1:1
	v_add_u32_e32 v0, 0x18c0, v83

	ds_write2_b32 v0, v42, v43 offset1:1
	v_add_u32_e32 v0, 0x18c8, v83
	ds_write2_b32 v0, v44, v45 offset1:1
	v_add_u32_e32 v0, 0x1ce0, v83

	ds_write2_b32 v0, v34, v35 offset1:1
	v_add_u32_e32 v0, 0x1ce8, v83
	ds_write2_b32 v0, v36, v37 offset1:1
	s_waitcnt lgkmcnt(0)
	ds_read2_b32 v[34:35], v82 offset1:33
	ds_read2_b32 v[36:37], v82 offset0:66 offset1:99
	ds_read2_b32 v[42:43], v82 offset0:132 offset1:165
	ds_read2_b32 v[44:45], v82 offset0:198 offset1:231
	s_mov_b64 s[22:23], -1
	s_waitcnt lgkmcnt(3)
	v_pk_mul_f32 v[40:41], s[14:15], v[34:35] op_sel_hi:[0,1]
	s_waitcnt lgkmcnt(2)
	v_pk_mul_f32 v[38:39], s[14:15], v[36:37] op_sel_hi:[0,1]
	s_waitcnt lgkmcnt(1)
	v_pk_mul_f32 v[36:37], s[14:15], v[42:43] op_sel_hi:[0,1]
	s_waitcnt lgkmcnt(0)
	v_pk_mul_f32 v[34:35], s[14:15], v[44:45] op_sel_hi:[0,1]
	s_mov_b64 s[18:19], 0
	s_cmp_lt_i32 s39, 2
	s_mov_b64 s[20:21], 0
	s_cbranch_scc1 .LBB0_638
	s_cmp_eq_u32 s39, 2
	s_mov_b64 s[20:21], -1
	s_cbranch_scc0 .LBB0_635
	v_rndne_f32_e32 v42, v41
	v_rndne_f32_e32 v43, v38
	v_rndne_f32_e32 v0, v40
	v_cvt_i32_f32_e32 v42, v42
	v_cvt_i32_f32_e32 v43, v43
	v_rndne_f32_e32 v44, v39
	v_cvt_i32_f32_e32 v0, v0
	v_cvt_i32_f32_e32 v44, v44
	v_med3_i32 v42, v42, s84, v236
	v_med3_i32 v43, v43, s84, v236
	v_med3_i32 v0, v0, s84, v236
	v_med3_i32 v44, v44, s84, v236
	v_lshlrev_b32_e32 v42, 8, v42
	v_lshlrev_b32_e32 v43, 16, v43
	v_and_b32_e32 v42, 0xff00, v42
	v_and_b32_e32 v43, 0xff0000, v43
	v_perm_b32 v0, v44, v0, s60
	v_or3_b32 v42, v0, v42, v43
	v_rndne_f32_e32 v43, v37
	v_rndne_f32_e32 v44, v34
	v_rndne_f32_e32 v0, v36
	v_cvt_i32_f32_e32 v43, v43
	v_cvt_i32_f32_e32 v44, v44
	v_rndne_f32_e32 v45, v35
	v_cvt_i32_f32_e32 v0, v0
	v_cvt_i32_f32_e32 v45, v45
	v_med3_i32 v43, v43, s84, v236
	v_med3_i32 v44, v44, s84, v236
	v_med3_i32 v0, v0, s84, v236
	v_med3_i32 v45, v45, s84, v236
	v_lshlrev_b32_e32 v43, 8, v43
	v_lshlrev_b32_e32 v44, 16, v44
	v_and_b32_e32 v43, 0xff00, v43
	v_and_b32_e32 v44, 0xff0000, v44
	v_perm_b32 v0, v45, v0, s60
	v_or3_b32 v43, v0, v43, v44
	v_mov_b64_e32 v[44:45], s[10:11]
	v_mad_i64_i32 v[44:45], s[4:5], s38, v66, v[44:45]
	v_lshl_add_u64 v[44:45], v[44:45], 0, v[76:77]
	global_store_dwordx2 v[44:45], v[42:43], off
	s_mov_b64 s[20:21], 0

.LBB0_672:
	s_waitcnt lgkmcnt(0)
	s_andn2_b64 vcc, exec, s[16:17]
	s_mov_b64 s[10:11], -1
	s_cbranch_vccnz .LBB0_624
	v_readlane_b32 s4, v254, 31
	s_add_i32 s37, s37, s42
	s_add_i32 s36, s36, s65
	s_add_i32 s35, s35, s4
	s_mov_b64 s[10:11], 0
	s_waitcnt vmcnt(4)
	v_mov_b32_e32 v37, v29
	v_mov_b32_e32 v36, v28
	v_mov_b32_e32 v35, v27
	v_mov_b32_e32 v34, v26
	v_mov_b32_e32 v45, v33
	v_mov_b32_e32 v44, v32
	v_mov_b32_e32 v43, v31
	v_mov_b32_e32 v42, v30
	v_mov_b32_e32 v41, v21
	v_mov_b32_e32 v40, v20
	v_mov_b32_e32 v39, v19
	v_mov_b32_e32 v38, v18
	v_mov_b32_e32 v53, v25
	v_mov_b32_e32 v52, v24
	v_mov_b32_e32 v51, v23
	v_mov_b32_e32 v50, v22
	v_mov_b32_e32 v49, v13
	v_mov_b32_e32 v48, v12
	v_mov_b32_e32 v47, v11
	v_mov_b32_e32 v46, v10
	v_mov_b32_e32 v61, v17
	v_mov_b32_e32 v60, v16
	v_mov_b32_e32 v59, v15
	v_mov_b32_e32 v58, v14
	v_mov_b32_e32 v57, v5
	v_mov_b32_e32 v56, v4
	v_mov_b32_e32 v55, v3
	v_mov_b32_e32 v54, v2
	v_mov_b32_e32 v65, v9
	v_mov_b32_e32 v64, v8
	v_mov_b32_e32 v63, v7
	v_mov_b32_e32 v62, v6
	s_branch .LBB0_624

.LBB0_691:
	v_add_u32_e32 v0, 0x420, v90

	ds_write2_b32 v90, v62, v63 offset1:1
	ds_write2_b32 v90, v64, v65 offset0:2 offset1:3

	ds_write2_b32 v0, v54, v55 offset1:1
	v_add_u32_e32 v0, 0x428, v90
	ds_write2_b32 v0, v56, v57 offset1:1
	v_add_u32_e32 v0, 0x840, v90

	ds_write2_b32 v0, v58, v59 offset1:1
	v_add_u32_e32 v0, 0x848, v90
	ds_write2_b32 v0, v60, v61 offset1:1
	v_add_u32_e32 v0, 0xc60, v90

	ds_write2_b32 v0, v46, v47 offset1:1
	v_add_u32_e32 v0, 0xc68, v90
	ds_write2_b32 v0, v48, v49 offset1:1
	v_add_u32_e32 v0, 0x1080, v90

	ds_write2_b32 v0, v50, v51 offset1:1
	v_add_u32_e32 v0, 0x1088, v90
	ds_write2_b32 v0, v52, v53 offset1:1
	v_add_u32_e32 v0, 0x14a0, v90

	ds_write2_b32 v0, v38, v39 offset1:1
	v_add_u32_e32 v0, 0x14a8, v90
	ds_write2_b32 v0, v40, v41 offset1:1
	v_add_u32_e32 v0, 0x18c0, v90

	ds_write2_b32 v0, v42, v43 offset1:1
	v_add_u32_e32 v0, 0x18c8, v90
	ds_write2_b32 v0, v44, v45 offset1:1
	v_add_u32_e32 v0, 0x1ce0, v90

	ds_write2_b32 v0, v34, v35 offset1:1
	v_add_u32_e32 v0, 0x1ce8, v90
	ds_write2_b32 v0, v36, v37 offset1:1
	s_waitcnt lgkmcnt(0)
	ds_read2_b32 v[34:35], v69 offset1:33
	ds_read2_b32 v[36:37], v69 offset0:66 offset1:99
	ds_read2_b32 v[42:43], v69 offset0:132 offset1:165
	ds_read2_b32 v[44:45], v69 offset0:198 offset1:231
	s_mov_b64 s[14:15], -1
	s_waitcnt lgkmcnt(3)
	v_pk_mul_f32 v[40:41], v[86:87], v[34:35] op_sel_hi:[0,1]
	s_waitcnt lgkmcnt(2)
	v_pk_mul_f32 v[38:39], v[86:87], v[36:37] op_sel_hi:[0,1]
	s_waitcnt lgkmcnt(1)
	v_pk_mul_f32 v[36:37], v[86:87], v[42:43] op_sel_hi:[0,1]
	s_waitcnt lgkmcnt(0)
	v_pk_mul_f32 v[34:35], v[86:87], v[44:45] op_sel_hi:[0,1]
	s_mov_b64 s[10:11], 0
	s_cmp_lt_i32 s28, 2
	s_mov_b64 s[12:13], 0
	s_cbranch_scc1 .LBB0_697
	s_cmp_eq_u32 s28, 2
	s_mov_b64 s[12:13], -1
	s_cbranch_scc0 .LBB0_694
	v_rndne_f32_e32 v42, v41
	v_rndne_f32_e32 v43, v38
	v_rndne_f32_e32 v0, v40
	v_cvt_i32_f32_e32 v42, v42
	v_cvt_i32_f32_e32 v43, v43
	v_rndne_f32_e32 v44, v39
	v_cvt_i32_f32_e32 v0, v0
	v_cvt_i32_f32_e32 v44, v44
	v_med3_i32 v42, v42, s84, v236
	v_med3_i32 v43, v43, s84, v236
	v_med3_i32 v0, v0, s84, v236
	v_med3_i32 v44, v44, s84, v236
	v_lshlrev_b32_e32 v42, 8, v42
	v_lshlrev_b32_e32 v43, 16, v43
	v_and_b32_e32 v42, 0xff00, v42
	v_and_b32_e32 v43, 0xff0000, v43
	v_perm_b32 v0, v44, v0, s60
	v_or3_b32 v42, v0, v42, v43
	v_rndne_f32_e32 v43, v37
	v_rndne_f32_e32 v44, v34
	v_rndne_f32_e32 v0, v36
	v_cvt_i32_f32_e32 v43, v43
	v_cvt_i32_f32_e32 v44, v44
	v_rndne_f32_e32 v45, v35
	v_cvt_i32_f32_e32 v0, v0
	v_cvt_i32_f32_e32 v45, v45
	v_med3_i32 v43, v43, s84, v236
	v_med3_i32 v44, v44, s84, v236
	v_med3_i32 v0, v0, s84, v236
	v_med3_i32 v45, v45, s84, v236
	v_lshlrev_b32_e32 v43, 8, v43
	v_lshlrev_b32_e32 v44, 16, v44
	v_and_b32_e32 v43, 0xff00, v43
	v_and_b32_e32 v44, 0xff0000, v44
	v_perm_b32 v0, v45, v0, s60
	v_or3_b32 v43, v0, v43, v44
	v_mad_i64_i32 v[44:45], s[4:5], v91, v68, v[80:81]
	v_lshl_add_u64 v[44:45], v[44:45], 0, v[78:79]
	global_store_dwordx2 v[44:45], v[42:43], off
	s_mov_b64 s[12:13], 0
